# baseline (speedup 1.0000x reference)
_Z7k_stageILi0ELi8EEv8AttnArgsPKDF16_PKfPDF16_iii:
	v_readfirstlane_b32 s94, v0
	s_nop 0
	s_lshr_b32 s94, s94, 6
	s_load_dwordx2 s[80:81], s[0:1], 0x70
	s_load_dwordx2 s[82:83], s[0:1], 0x88
	s_load_dwordx16 s[64:79], s[0:1], 0x0
	v_and_b32_e32 v255, 63, v0
	v_lshlrev_b32_e32 v255, 7, v255
	s_load_dwordx4 s[8:11], s[0:1], 0x88
	s_lshl_b32 s4, s2, 4
	s_and_b32 s4, s4, 0x70
	s_lshr_b32 s5, s2, 3
	s_add_i32 s4, s4, s5
	s_lshr_b32 s7, s4, 5
	s_lshl_b32 s6, s4, 1
	s_waitcnt lgkmcnt(0)
	s_mul_i32 s84, s3, s83
	s_add_i32 s84, s84, s82
	s_mul_i32 s84, s84, 0x60000
	s_mul_i32 s85, s94, 0x6000
	s_add_u32 s84, s84, s85
	s_add_u32 s80, s80, s84
	s_addc_u32 s81, s81, 0
	global_load_dword v254, v255, s[80:81]
	s_add_u32 s80, s80, 0x2000
	s_addc_u32 s81, s81, 0
	global_load_dword v254, v255, s[80:81]
	s_add_u32 s80, s80, 0x2000
	s_addc_u32 s81, s81, 0
	global_load_dword v254, v255, s[80:81]
	s_add_u32 s80, s80, 0x2c000
	s_addc_u32 s81, s81, 0
	global_load_dword v254, v255, s[80:81]
	s_add_u32 s80, s80, 0x2000
	s_addc_u32 s81, s81, 0
	global_load_dword v254, v255, s[80:81]
	s_add_u32 s80, s80, 0x2000
	s_addc_u32 s81, s81, 0
	global_load_dword v254, v255, s[80:81]
	s_lshl_b32 s11, s2, 1
	s_cmp_gt_i32 s10, 0
	v_readfirstlane_b32 s24, v0
	s_cbranch_scc1 .LBB3_2
	s_lshl_b32 s31, s7, 12
	s_ashr_i32 s2, s3, 31
	s_mov_b64 s[4:5], 0
	s_branch .LBB3_3

	.amdhsa_kernel _Z7k_stageILi0ELi8EEv8AttnArgsPKDF16_PKfPDF16_iii
		.amdhsa_group_segment_fixed_size 115712
		.amdhsa_private_segment_fixed_size 0
		.amdhsa_kernarg_size 148
		.amdhsa_user_sgpr_count 2
		.amdhsa_user_sgpr_dispatch_ptr 0
		.amdhsa_user_sgpr_queue_ptr 0
		.amdhsa_user_sgpr_kernarg_segment_ptr 1
		.amdhsa_user_sgpr_dispatch_id 0
		.amdhsa_user_sgpr_kernarg_preload_length 0
		.amdhsa_user_sgpr_kernarg_preload_offset 0
		.amdhsa_user_sgpr_private_segment_size 0
		.amdhsa_uses_dynamic_stack 0
		.amdhsa_enable_private_segment 0
		.amdhsa_system_sgpr_workgroup_id_x 1
		.amdhsa_system_sgpr_workgroup_id_y 1
		.amdhsa_system_sgpr_workgroup_id_z 0
		.amdhsa_system_sgpr_workgroup_info 0
		.amdhsa_system_vgpr_workitem_id 0
		.amdhsa_next_free_vgpr 256
		.amdhsa_next_free_sgpr 96
		.amdhsa_accum_offset 256
		.amdhsa_reserve_vcc 1
		.amdhsa_float_round_mode_32 0
		.amdhsa_float_round_mode_16_64 0
		.amdhsa_float_denorm_mode_32 3
		.amdhsa_float_denorm_mode_16_64 3
		.amdhsa_dx10_clamp 1
		.amdhsa_ieee_mode 1
		.amdhsa_fp16_overflow 0
		.amdhsa_tg_split 0
		.amdhsa_exception_fp_ieee_invalid_op 0
		.amdhsa_exception_fp_denorm_src 0
		.amdhsa_exception_fp_ieee_div_zero 0
		.amdhsa_exception_fp_ieee_overflow 0
		.amdhsa_exception_fp_ieee_underflow 0
		.amdhsa_exception_fp_ieee_inexact 0
		.amdhsa_exception_int_div_zero 0
	.end_amdhsa_kernel

_Z7k_stageILi1ELi4EEv8AttnArgsPKDF16_PKfPDF16_iii:
	v_readfirstlane_b32 s94, v0
	s_nop 0
	s_lshr_b32 s94, s94, 6
	s_load_dwordx2 s[80:81], s[0:1], 0x70
	s_load_dwordx2 s[82:83], s[0:1], 0x88
	s_load_dwordx16 s[64:79], s[0:1], 0x0
	v_and_b32_e32 v255, 63, v0
	v_lshlrev_b32_e32 v255, 7, v255
	s_load_dwordx4 s[28:31], s[0:1], 0x70
	s_load_dwordx2 s[24:25], s[0:1], 0x80
	s_load_dword s33, s[0:1], 0x90
	s_lshl_b32 s4, s2, 5
	s_and_b32 s45, s4, 0xe0
	s_lshr_b32 s4, s2, 3
	s_add_i32 s45, s45, s4
	s_and_b32 s44, s2, 56
	v_readfirstlane_b32 s3, v0
	v_and_b32_e32 v1, 15, v0
	s_waitcnt lgkmcnt(0)
	s_mul_i32 s84, s3, s83
	s_add_i32 s84, s84, s82
	s_mul_i32 s84, s84, 0x60000
	s_mul_i32 s85, s94, 0x6000
	s_add_u32 s84, s84, s85
	s_add_u32 s80, s80, s84
	s_addc_u32 s81, s81, 0
	global_load_dword v254, v255, s[80:81]
	s_add_u32 s80, s80, 0x2000
	s_addc_u32 s81, s81, 0
	global_load_dword v254, v255, s[80:81]
	s_add_u32 s80, s80, 0x2000
	s_addc_u32 s81, s81, 0
	global_load_dword v254, v255, s[80:81]
	s_add_u32 s80, s80, 0x2c000
	s_addc_u32 s81, s81, 0
	global_load_dword v254, v255, s[80:81]
	s_add_u32 s80, s80, 0x2000
	s_addc_u32 s81, s81, 0
	global_load_dword v254, v255, s[80:81]
	s_add_u32 s80, s80, 0x2000
	s_addc_u32 s81, s81, 0
	global_load_dword v254, v255, s[80:81]
	s_cmp_lt_i32 s33, 1
	v_bfe_u32 v167, v0, 4, 2
	s_cbranch_scc1 .LBB4_155
	s_lshr_b32 s2, s3, 2
	v_lshrrev_b32_e32 v7, 7, v0
	v_lshrrev_b32_e32 v2, 5, v0
	v_lshrrev_b32_e32 v3, 4, v0
	s_and_b32 s2, s2, 16
	v_lshrrev_b32_e32 v4, 6, v0
	v_and_b32_e32 v7, 1, v7
	v_and_b32_e32 v2, 4, v2
	v_or_b32_e32 v179, s2, v1
	v_and_b32_e32 v5, 4, v4
	s_load_dwordx2 s[40:41], s[0:1], 0x60
	s_bitcmp1_b32 s3, 6
	v_lshlrev_b16_e32 v7, 2, v7
	v_and_b32_e32 v8, 3, v3
	s_load_dwordx4 s[36:39], s[0:1], 0x0
	s_load_dwordx2 s[4:5], s[0:1], 0x10
	s_load_dwordx8 s[8:15], s[0:1], 0x18
	s_load_dwordx2 s[6:7], s[0:1], 0x38
	s_load_dwordx8 s[16:23], s[0:1], 0x40
	v_or_b32_e32 v178, v2, v167
	v_and_or_b32 v180, s45, 56, v5
	s_cselect_b64 s[26:27], -1, 0
	s_and_b32 s3, s45, 0x3ffffc0
	v_bitop3_b16 v3, v7, v3, 3 bitop3:0xf8
	v_bitop3_b16 v7, v7, 8, v8 bitop3:0xfe
	v_lshlrev_b32_e32 v8, 12, v5
	v_bitop3_b32 v2, v2, v179, v167 bitop3:0x36
	v_or_b32_e32 v6, s3, v180
	s_and_b32 s3, s45, 0x1ffc0
	v_and_b32_e32 v3, 0xffff, v3
	v_lshl_or_b32 v184, v2, 4, v8
	v_lshlrev_b32_e32 v2, 3, v5
	v_mov_b32_e32 v169, 0
	v_lshlrev_b32_e32 v168, 5, v179
	v_lshlrev_b32_e32 v181, 6, v6
	v_or_b32_e32 v6, s3, v180
	v_and_b32_e32 v7, 0xffff, v7
	v_or_b32_e32 v186, 8, v2
	v_or_b32_e32 v188, 16, v2
	v_bitop3_b32 v2, s2, v3, v1 bitop3:0x36
	v_lshlrev_b32_e32 v166, 3, v179
	s_waitcnt lgkmcnt(0)
	v_lshl_add_u64 v[170:171], s[38:39], 0, v[168:169]
	s_mov_b32 s39, 0x20000
	v_lshlrev_b32_e32 v189, 4, v2
	v_bitop3_b32 v2, s2, v7, v1 bitop3:0x36
	v_lshlrev_b32_e32 v193, 15, v6
	v_lshl_add_u64 v[172:173], s[4:5], 0, v[168:169]
	s_and_b32 s37, s37, 0xffff
	s_mov_b32 s38, 0x1800000
	v_add_u32_e32 v182, -1, v180
	v_add_u32_e32 v183, 4, v180
	v_lshl_add_u64 v[174:175], s[14:15], 0, v[168:169]
	v_lshl_add_u64 v[176:177], s[6:7], 0, v[168:169]
	s_and_b32 s13, s13, 0xffff
	s_mov_b32 s42, 0x800000
	s_mov_b32 s43, s39
	s_and_b32 s41, s41, 0xffff
	v_or_b32_e32 v185, 64, v181
	v_or_b32_e32 v187, 0x80, v181
	v_or_b32_e32 v190, 0xc0, v181
	v_lshl_or_b32 v191, v4, 3, 24
	v_lshlrev_b32_e32 v192, 4, v2
	v_lshlrev_b32_e32 v194, 4, v179
	v_or_b32_e32 v195, 0x8000, v193
	v_or_b32_e32 v196, 0x10000, v193
	v_or_b32_e32 v197, 0x18000, v193
	s_mov_b32 s46, 0
	s_movk_i32 s47, 0x300
	v_lshlrev_b32_e32 v198, 1, v166
	s_branch .LBB4_4

	.amdhsa_kernel _Z7k_stageILi1ELi4EEv8AttnArgsPKDF16_PKfPDF16_iii
		.amdhsa_group_segment_fixed_size 82944
		.amdhsa_private_segment_fixed_size 0
		.amdhsa_kernarg_size 148
		.amdhsa_user_sgpr_count 2
		.amdhsa_user_sgpr_dispatch_ptr 0
		.amdhsa_user_sgpr_queue_ptr 0
		.amdhsa_user_sgpr_kernarg_segment_ptr 1
		.amdhsa_user_sgpr_dispatch_id 0
		.amdhsa_user_sgpr_kernarg_preload_length 0
		.amdhsa_user_sgpr_kernarg_preload_offset 0
		.amdhsa_user_sgpr_private_segment_size 0
		.amdhsa_uses_dynamic_stack 0
		.amdhsa_enable_private_segment 0
		.amdhsa_system_sgpr_workgroup_id_x 1
		.amdhsa_system_sgpr_workgroup_id_y 0
		.amdhsa_system_sgpr_workgroup_id_z 0
		.amdhsa_system_sgpr_workgroup_info 0
		.amdhsa_system_vgpr_workitem_id 0
		.amdhsa_next_free_vgpr 256
		.amdhsa_next_free_sgpr 96
		.amdhsa_accum_offset 256
		.amdhsa_reserve_vcc 1
		.amdhsa_float_round_mode_32 0
		.amdhsa_float_round_mode_16_64 0
		.amdhsa_float_denorm_mode_32 3
		.amdhsa_float_denorm_mode_16_64 3
		.amdhsa_dx10_clamp 1
		.amdhsa_ieee_mode 1
		.amdhsa_fp16_overflow 0
		.amdhsa_tg_split 0
		.amdhsa_exception_fp_ieee_invalid_op 0
		.amdhsa_exception_fp_denorm_src 0
		.amdhsa_exception_fp_ieee_div_zero 0
		.amdhsa_exception_fp_ieee_overflow 0
		.amdhsa_exception_fp_ieee_underflow 0
		.amdhsa_exception_fp_ieee_inexact 0
		.amdhsa_exception_int_div_zero 0
	.end_amdhsa_kernel

_Z7k_stageILi0ELi4EEv8AttnArgsPKDF16_PKfPDF16_iii:
	v_readfirstlane_b32 s94, v0
	s_nop 0
	s_lshr_b32 s94, s94, 6
	s_load_dwordx2 s[80:81], s[0:1], 0x70
	s_load_dwordx2 s[82:83], s[0:1], 0x88
	s_load_dwordx16 s[64:79], s[0:1], 0x0
	v_and_b32_e32 v255, 63, v0
	v_lshlrev_b32_e32 v255, 7, v255
	s_load_dwordx4 s[8:11], s[0:1], 0x70
	s_load_dwordx2 s[20:21], s[0:1], 0x80
	s_load_dwordx4 s[12:15], s[0:1], 0x88
	s_lshl_b32 s5, s2, 5
	s_waitcnt lgkmcnt(0)
	s_mul_i32 s84, s3, s83
	s_add_i32 s84, s84, s82
	s_mul_i32 s84, s84, 0x60000
	s_mul_i32 s85, s94, 0x6000
	s_add_u32 s84, s84, s85
	s_add_u32 s80, s80, s84
	s_addc_u32 s81, s81, 0
	global_load_dword v254, v255, s[80:81]
	s_add_u32 s80, s80, 0x2000
	s_addc_u32 s81, s81, 0
	global_load_dword v254, v255, s[80:81]
	s_add_u32 s80, s80, 0x2000
	s_addc_u32 s81, s81, 0
	global_load_dword v254, v255, s[80:81]
	s_add_u32 s80, s80, 0x2c000
	s_addc_u32 s81, s81, 0
	global_load_dword v254, v255, s[80:81]
	s_add_u32 s80, s80, 0x2000
	s_addc_u32 s81, s81, 0
	global_load_dword v254, v255, s[80:81]
	s_add_u32 s80, s80, 0x2000
	s_addc_u32 s81, s81, 0
	global_load_dword v254, v255, s[80:81]
	s_and_b32 s15, s5, 0xe0
	s_lshr_b32 s5, s2, 3
	s_add_i32 s15, s15, s5
	s_and_b32 s2, s2, 56
	v_readfirstlane_b32 s4, v0
	v_and_b32_e32 v1, 15, v0
	s_cmp_lt_i32 s14, 1
	v_bfe_u32 v158, v0, 4, 2
	s_cbranch_scc1 .LBB5_79
	s_bfe_u32 s5, s4, 0x10006
	s_lshl_b32 s6, s5, 4
	s_mul_i32 s16, s3, 40
	s_mul_hi_i32 s7, s3, 40
	s_add_u32 s22, s0, s16
	s_addc_u32 s23, s1, s7
	s_load_dwordx4 s[16:19], s[22:23], 0x0
	s_load_dwordx2 s[0:1], s[22:23], 0x10
	v_or_b32_e32 v159, s6, v1
	v_lshlrev_b32_e32 v18, 5, v159
	s_waitcnt lgkmcnt(0)
	global_load_dwordx4 v[2:5], v18, s[18:19]
	global_load_dwordx4 v[6:9], v18, s[0:1]
	global_load_dwordx4 v[10:13], v18, s[18:19] offset:16
	global_load_dwordx4 v[14:17], v18, s[0:1] offset:16
	v_bfe_u32 v21, v0, 7, 1
	v_lshrrev_b32_e32 v19, 4, v0
	v_lshlrev_b16_e32 v23, 2, v21
	v_lshrrev_b32_e32 v18, 5, v0
	v_lshrrev_b32_e32 v20, 6, v0
	v_and_b32_e32 v24, 3, v19
	v_bitop3_b16 v19, v23, v19, 3 bitop3:0xf8
	s_movk_i32 s0, 0x3000
	v_and_b32_e32 v18, 4, v18
	v_and_b32_e32 v22, 4, v20
	v_lshlrev_b32_e32 v20, 12, v20
	v_lshlrev_b32_e32 v21, 11, v21
	v_and_b32_e32 v19, 0xffff, v19
	s_bitcmp1_b32 s4, 6
	v_or_b32_e32 v161, v18, v158
	v_and_or_b32 v162, s15, 56, v22
	v_bitop3_b16 v23, v23, 8, v24 bitop3:0xfe
	v_lshlrev_b32_e32 v24, 3, v22
	v_lshl_or_b32 v22, v22, 12, v21
	v_or3_b32 v163, v20, v21, s0
	v_bitop3_b32 v18, v18, v159, v158 bitop3:0x36
	v_bitop3_b32 v19, s6, v19, v1 bitop3:0x36
	s_cselect_b64 s[24:25], -1, 0
	s_and_b32 s0, s15, 0x1ffc0
	s_movk_i32 s1, 0x2000
	v_lshl_or_b32 v168, v18, 4, v22
	v_lshlrev_b32_e32 v18, 4, v19
	v_or_b32_e32 v19, s0, v162
	v_add3_u32 v170, v22, v18, s1
	v_lshl_or_b32 v18, v19, 6, s2
	v_add_u32_e32 v18, v161, v18
	v_mul_u32_u24_e32 v18, 0x600, v18
	v_and_b32_e32 v20, 0xffff, v23
	v_lshl_or_b32 v18, s5, 8, v18
	v_lshlrev_b32_e32 v160, 9, v158
	v_bitop3_b32 v20, s6, v20, v1 bitop3:0x36
	v_lshl_or_b32 v18, v1, 4, v18
	v_add_u32_e32 v164, -1, v162
	v_add_u32_e32 v165, 4, v162
	v_or3_b32 v166, v161, v24, 8
	v_or_b32_e32 v167, 0x1000, v22
	v_lshl_or_b32 v169, v20, 4, v160
	s_and_b32 s17, s17, 0xffff
	s_mov_b32 s19, 0x20000
	s_mov_b32 s18, 0x1800000
	v_add_u32_e32 v171, 0xfffe7c00, v18
	s_mov_b32 s30, s2
	s_waitcnt vmcnt(3)
	v_cvt_pk_f16_f32 v172, v2, v3
	s_waitcnt vmcnt(2)
	v_cvt_pk_f16_f32 v173, v6, v7
	v_cvt_pk_f16_f32 v174, v4, v5
	v_cvt_pk_f16_f32 v175, v8, v9
	s_waitcnt vmcnt(1)
	v_cvt_pk_f16_f32 v176, v10, v11
	s_waitcnt vmcnt(0)
	v_cvt_pk_f16_f32 v177, v14, v15
	v_cvt_pk_f16_f32 v178, v12, v13
	v_cvt_pk_f16_f32 v179, v16, v17
	s_branch .LBB5_4

	.amdhsa_kernel _Z7k_stageILi0ELi4EEv8AttnArgsPKDF16_PKfPDF16_iii
		.amdhsa_group_segment_fixed_size 82944
		.amdhsa_private_segment_fixed_size 0
		.amdhsa_kernarg_size 148
		.amdhsa_user_sgpr_count 2
		.amdhsa_user_sgpr_dispatch_ptr 0
		.amdhsa_user_sgpr_queue_ptr 0
		.amdhsa_user_sgpr_kernarg_segment_ptr 1
		.amdhsa_user_sgpr_dispatch_id 0
		.amdhsa_user_sgpr_kernarg_preload_length 0
		.amdhsa_user_sgpr_kernarg_preload_offset 0
		.amdhsa_user_sgpr_private_segment_size 0
		.amdhsa_uses_dynamic_stack 0
		.amdhsa_enable_private_segment 0
		.amdhsa_system_sgpr_workgroup_id_x 1
		.amdhsa_system_sgpr_workgroup_id_y 1
		.amdhsa_system_sgpr_workgroup_id_z 0
		.amdhsa_system_sgpr_workgroup_info 0
		.amdhsa_system_vgpr_workitem_id 0
		.amdhsa_next_free_vgpr 256
		.amdhsa_next_free_sgpr 96
		.amdhsa_accum_offset 256
		.amdhsa_reserve_vcc 1
		.amdhsa_float_round_mode_32 0
		.amdhsa_float_round_mode_16_64 0
		.amdhsa_float_denorm_mode_32 3
		.amdhsa_float_denorm_mode_16_64 3
		.amdhsa_dx10_clamp 1
		.amdhsa_ieee_mode 1
		.amdhsa_fp16_overflow 0
		.amdhsa_tg_split 0
		.amdhsa_exception_fp_ieee_invalid_op 0
		.amdhsa_exception_fp_denorm_src 0
		.amdhsa_exception_fp_ieee_div_zero 0
		.amdhsa_exception_fp_ieee_overflow 0
		.amdhsa_exception_fp_ieee_underflow 0
		.amdhsa_exception_fp_ieee_inexact 0
		.amdhsa_exception_int_div_zero 0
	.end_amdhsa_kernel

amdhsa.kernels:
  - .agpr_count:     0
    .args:
      - .actual_access:  read_only
        .address_space:  global
        .offset:         0
        .size:           8
        .value_kind:     global_buffer
      - .actual_access:  read_only
        .address_space:  global
        .offset:         8
        .size:           8
        .value_kind:     global_buffer
      - .actual_access:  read_only
        .address_space:  global
        .offset:         16
        .size:           8
        .value_kind:     global_buffer
      - .actual_access:  read_only
        .address_space:  global
        .offset:         24
        .size:           8
        .value_kind:     global_buffer
      - .actual_access:  read_only
        .address_space:  global
        .offset:         32
        .size:           8
        .value_kind:     global_buffer
      - .actual_access:  read_only
        .address_space:  global
        .offset:         40
        .size:           8
        .value_kind:     global_buffer
      - .actual_access:  read_only
        .address_space:  global
        .offset:         48
        .size:           8
        .value_kind:     global_buffer
      - .actual_access:  read_only
        .address_space:  global
        .offset:         56
        .size:           8
        .value_kind:     global_buffer
      - .actual_access:  write_only
        .address_space:  global
        .offset:         64
        .size:           8
        .value_kind:     global_buffer
      - .actual_access:  write_only
        .address_space:  global
        .offset:         72
        .size:           8
        .value_kind:     global_buffer
      - .actual_access:  write_only
        .address_space:  global
        .offset:         80
        .size:           8
        .value_kind:     global_buffer
      - .actual_access:  write_only
        .address_space:  global
        .offset:         88
        .size:           8
        .value_kind:     global_buffer
    .group_segment_fixed_size: 0
    .kernarg_segment_align: 8
    .kernarg_segment_size: 96
    .language:       OpenCL C
    .language_version:
      - 2
      - 0
    .max_flat_workgroup_size: 256
    .name:           _Z8k_prep_wPKfS0_S0_S0_S0_S0_S0_S0_PDF16_PfS1_S1_
    .private_segment_fixed_size: 0
    .sgpr_count:     23
    .sgpr_spill_count: 0
    .symbol:         _Z8k_prep_wPKfS0_S0_S0_S0_S0_S0_S0_PDF16_PfS1_S1_.kd
    .uniform_work_group_size: 1
    .uses_dynamic_stack: false
    .vgpr_count:     15
    .vgpr_spill_count: 0
    .wavefront_size: 64
  - .agpr_count:     0
    .args:
      - .actual_access:  read_only
        .address_space:  global
        .offset:         0
        .size:           8
        .value_kind:     global_buffer
      - .actual_access:  read_only
        .address_space:  global
        .offset:         8
        .size:           8
        .value_kind:     global_buffer
      - .actual_access:  read_only
        .address_space:  global
        .offset:         16
        .size:           8
        .value_kind:     global_buffer
      - .actual_access:  read_only
        .address_space:  global
        .offset:         24
        .size:           8
        .value_kind:     global_buffer
      - .actual_access:  write_only
        .address_space:  global
        .offset:         32
        .size:           8
        .value_kind:     global_buffer
      - .actual_access:  read_only
        .address_space:  global
        .offset:         40
        .size:           8
        .value_kind:     global_buffer
      - .actual_access:  read_only
        .address_space:  global
        .offset:         48
        .size:           8
        .value_kind:     global_buffer
      - .actual_access:  write_only
        .address_space:  global
        .offset:         56
        .size:           8
        .value_kind:     global_buffer
      - .offset:         64
        .size:           4
        .value_kind:     by_value
      - .offset:         68
        .size:           4
        .value_kind:     by_value
    .group_segment_fixed_size: 115712
    .kernarg_segment_align: 8
    .kernarg_segment_size: 72
    .language:       OpenCL C
    .language_version:
      - 2
      - 0
    .max_flat_workgroup_size: 512
    .name:           _Z8k_stageAPKfS0_S0_S0_PDF16_PKDF16_S0_S1_ii
    .private_segment_fixed_size: 0
    .sgpr_count:     28
    .sgpr_spill_count: 0
    .symbol:         _Z8k_stageAPKfS0_S0_S0_PDF16_PKDF16_S0_S1_ii.kd
    .uniform_work_group_size: 1
    .uses_dynamic_stack: false
    .vgpr_count:     251
    .vgpr_spill_count: 0
    .wavefront_size: 64
  - .agpr_count:     112
    .args:
      - .actual_access:  read_only
        .address_space:  global
        .offset:         0
        .size:           8
        .value_kind:     global_buffer
      - .actual_access:  read_only
        .address_space:  global
        .offset:         8
        .size:           8
        .value_kind:     global_buffer
      - .actual_access:  read_only
        .address_space:  global
        .offset:         16
        .size:           8
        .value_kind:     global_buffer
      - .actual_access:  read_only
        .address_space:  global
        .offset:         24
        .size:           8
        .value_kind:     global_buffer
      - .actual_access:  read_only
        .address_space:  global
        .offset:         32
        .size:           8
        .value_kind:     global_buffer
      - .actual_access:  write_only
        .address_space:  global
        .offset:         40
        .size:           8
        .value_kind:     global_buffer
    .group_segment_fixed_size: 107712
    .kernarg_segment_align: 8
    .kernarg_segment_size: 48
    .language:       OpenCL C
    .language_version:
      - 2
      - 0
    .max_flat_workgroup_size: 256
    .name:           _Z7k_conv4PKDF16_S0_S0_PKfS2_Pf
    .private_segment_fixed_size: 0
    .sgpr_count:     36
    .sgpr_spill_count: 0
    .symbol:         _Z7k_conv4PKDF16_S0_S0_PKfS2_Pf.kd
    .uniform_work_group_size: 1
    .uses_dynamic_stack: false
    .vgpr_count:     328
    .vgpr_spill_count: 0
    .wavefront_size: 64
  - .agpr_count:     0
    .args:
      - .offset:         0
        .size:           112
        .value_kind:     by_value
      - .actual_access:  read_only
        .address_space:  global
        .offset:         112
        .size:           8
        .value_kind:     global_buffer
      - .actual_access:  read_only
        .address_space:  global
        .offset:         120
        .size:           8
        .value_kind:     global_buffer
      - .actual_access:  write_only
        .address_space:  global
        .offset:         128
        .size:           8
        .value_kind:     global_buffer
      - .offset:         136
        .size:           4
        .value_kind:     by_value
      - .offset:         140
        .size:           4
        .value_kind:     by_value
      - .offset:         144
        .size:           4
        .value_kind:     by_value
    .group_segment_fixed_size: 115712
    .kernarg_segment_align: 8
    .kernarg_segment_size: 148
    .language:       OpenCL C
    .language_version:
      - 2
      - 0
    .max_flat_workgroup_size: 512
    .name:           _Z7k_stageILi0ELi8EEv8AttnArgsPKDF16_PKfPDF16_iii
    .private_segment_fixed_size: 0
    .sgpr_count:     41
    .sgpr_spill_count: 0
    .symbol:         _Z7k_stageILi0ELi8EEv8AttnArgsPKDF16_PKfPDF16_iii.kd
    .uniform_work_group_size: 1
    .uses_dynamic_stack: false
    .vgpr_count:     256
    .vgpr_spill_count: 0
    .wavefront_size: 64
  - .agpr_count:     0
    .args:
      - .offset:         0
        .size:           112
        .value_kind:     by_value
      - .actual_access:  read_only
        .address_space:  global
        .offset:         112
        .size:           8
        .value_kind:     global_buffer
      - .actual_access:  read_only
        .address_space:  global
        .offset:         120
        .size:           8
        .value_kind:     global_buffer
      - .actual_access:  write_only
        .address_space:  global
        .offset:         128
        .size:           8
        .value_kind:     global_buffer
      - .offset:         136
        .size:           4
        .value_kind:     by_value
      - .offset:         140
        .size:           4
        .value_kind:     by_value
      - .offset:         144
        .size:           4
        .value_kind:     by_value
    .group_segment_fixed_size: 82944
    .kernarg_segment_align: 8
    .kernarg_segment_size: 148
    .language:       OpenCL C
    .language_version:
      - 2
      - 0
    .max_flat_workgroup_size: 512
    .name:           _Z7k_stageILi1ELi4EEv8AttnArgsPKDF16_PKfPDF16_iii
    .private_segment_fixed_size: 0
    .sgpr_count:     55
    .sgpr_spill_count: 0
    .symbol:         _Z7k_stageILi1ELi4EEv8AttnArgsPKDF16_PKfPDF16_iii.kd
    .uniform_work_group_size: 1
    .uses_dynamic_stack: false
    .vgpr_count:     256
    .vgpr_spill_count: 0
    .wavefront_size: 64
  - .agpr_count:     0
    .args:
      - .offset:         0
        .size:           112
        .value_kind:     by_value
      - .actual_access:  read_only
        .address_space:  global
        .offset:         112
        .size:           8
        .value_kind:     global_buffer
      - .actual_access:  read_only
        .address_space:  global
        .offset:         120
        .size:           8
        .value_kind:     global_buffer
      - .actual_access:  write_only
        .address_space:  global
        .offset:         128
        .size:           8
        .value_kind:     global_buffer
      - .offset:         136
        .size:           4
        .value_kind:     by_value
      - .offset:         140
        .size:           4
        .value_kind:     by_value
      - .offset:         144
        .size:           4
        .value_kind:     by_value
    .group_segment_fixed_size: 82944
    .kernarg_segment_align: 8
    .kernarg_segment_size: 148
    .language:       OpenCL C
    .language_version:
      - 2
      - 0
    .max_flat_workgroup_size: 512
    .name:           _Z7k_stageILi0ELi4EEv8AttnArgsPKDF16_PKfPDF16_iii
    .private_segment_fixed_size: 0
    .sgpr_count:     38
    .sgpr_spill_count: 0
    .symbol:         _Z7k_stageILi0ELi4EEv8AttnArgsPKDF16_PKfPDF16_iii.kd
    .uniform_work_group_size: 1
    .uses_dynamic_stack: false
    .vgpr_count:     256
    .vgpr_spill_count: 0
    .wavefront_size: 64
  - .agpr_count:     0
    .args:
      - .offset:         0
        .size:           112
        .value_kind:     by_value
    .group_segment_fixed_size: 0
    .kernarg_segment_align: 8
    .kernarg_segment_size: 112
    .language:       OpenCL C
    .language_version:
      - 2
      - 0
    .max_flat_workgroup_size: 512
    .name:           _Z7k_attn2ILi2EEv8AttnArgs
    .private_segment_fixed_size: 0
    .sgpr_count:     86
    .sgpr_spill_count: 0
    .symbol:         _Z7k_attn2ILi2EEv8AttnArgs.kd
    .uniform_work_group_size: 1
    .uses_dynamic_stack: false
    .vgpr_count:     236
    .vgpr_spill_count: 0
    .wavefront_size: 64
